# speedup vs baseline: 1.0043x; 1.0043x over previous
_ZN2g34gemmILi4ELi1EEEvPKDF16_S2_PvPKfiiff:
	v_lshrrev_b32_e32 v1, 2, v0
	v_and_b32_e32 v1, 12, v1
	s_movk_i32 s18, 0x1320
	v_lshrrev_b32_e64 v1, v1, s18
	v_readfirstlane_b32 s16, v0
	v_xor_b32_e32 v1, v1, v0
	s_load_dword s12, s[0:1], 0x20
	s_load_dwordx8 s[4:11], s[0:1], 0x0
	s_lshr_b32 s17, s16, 6
	s_lshl_b32 s3, s2, 2
	v_lshlrev_b32_e32 v1, 4, v1
	v_lshlrev_b32_e32 v2, 4, v0
	s_and_b32 s14, s3, 28
	s_bfe_u32 s2, s2, 0x20003
	v_and_b32_e32 v1, 48, v1
	s_lshl_b32 s23, s17, 11
	v_and_b32_e32 v2, 0x3c0, v2
	s_or_b32 s24, s14, s2
	v_or3_b32 v100, s23, v2, v1
	v_lshrrev_b32_e32 v2, 1, v0
	s_lshr_b32 s2, s16, 2
	v_and_b32_e32 v2, 24, v2
	v_bfe_u32 v3, v0, 2, 2
	s_and_b32 s2, s2, 0x60
	s_waitcnt lgkmcnt(0)
	s_ashr_i32 s13, s12, 31
	s_lshr_b32 s14, s16, 4
	v_or3_b32 v2, v3, v2, s2
	s_and_b32 s2, s3, 0xffffff80
	s_lshl_b32 s3, s24, 14
	s_add_u32 s4, s4, s3
	s_addc_u32 s5, s5, 0
	s_ashr_i32 s3, s2, 31
	v_and_or_b32 v2, s14, 4, v2
	s_lshl_b64 s[14:15], s[2:3], 6
	s_add_u32 s6, s6, s14
	s_addc_u32 s7, s7, s15
	s_lshr_b32 s3, s16, 1
	s_and_b32 s22, s16, 64
	s_mov_b32 s16, m0
	s_mov_b32 m0, s23
	s_nop 0
	global_load_lds_dwordx4 v100, s[4:5]
	s_mov_b32 m0, s16
	v_or_b32_e32 v99, 0x400, v100
	s_lshl_b32 s25, s17, 10
	s_or_b32 s16, s23, 0x400
	s_mov_b32 s17, m0
	s_mov_b32 m0, s16
	s_nop 0
	global_load_lds_dwordx4 v99, s[4:5]
	s_mov_b32 m0, s17
	v_lshl_or_b32 v102, v2, 6, v1
	s_and_b32 s3, s3, 0x7fffffc0
	s_lshl_b64 s[14:15], s[12:13], 6
	s_add_i32 s26, s25, 0x4000
	s_mov_b32 s16, m0
	s_mov_b32 m0, s26
	s_nop 0
	global_load_lds_dwordx4 v102, s[6:7]
	s_mov_b32 m0, s16
	s_add_u32 s16, s4, 0x80000
	v_and_b32_e32 v96, 15, v0
	v_lshrrev_b32_e32 v97, 4, v0
	v_and_b32_e32 v0, 12, v0
	s_addc_u32 s17, s5, 0
	v_lshrrev_b32_e64 v0, v0, s18
	s_add_u32 s18, s6, s14
	s_addc_u32 s19, s7, s15
	s_add_i32 s20, s23, 0x6000
	s_mov_b32 s21, m0
	s_mov_b32 m0, s20
	s_nop 0
	global_load_lds_dwordx4 v100, s[16:17]
	s_mov_b32 m0, s21
	s_add_i32 s20, s23, 0x6400
	s_mov_b32 s21, m0
	s_mov_b32 m0, s20
	s_nop 0
	global_load_lds_dwordx4 v99, s[16:17]
	s_mov_b32 m0, s21
	s_add_i32 s16, s25, 0xa000
	s_mov_b32 s17, m0
	s_mov_b32 m0, s16
	s_nop 0
	global_load_lds_dwordx4 v102, s[18:19]
	s_mov_b32 m0, s17
	s_add_u32 s16, s4, 0x100000
	s_addc_u32 s17, s5, 0
	s_add_u32 s14, s18, s14
	v_xor_b32_e32 v0, v0, v97
	s_addc_u32 s15, s19, s15
	s_add_i32 s18, s23, 0xc000
	s_mov_b32 s19, m0
	s_mov_b32 m0, s18
	s_nop 0
	global_load_lds_dwordx4 v100, s[16:17]
	s_mov_b32 m0, s19
	v_lshlrev_b32_e32 v0, 4, v0
	s_add_i32 s18, s23, 0xc400
	s_mov_b32 s19, m0
	s_mov_b32 m0, s18
	s_nop 0
	global_load_lds_dwordx4 v99, s[16:17]
	s_mov_b32 m0, s19
	v_or_b32_e32 v1, s3, v96
	v_or_b32_e32 v4, s22, v96
	v_and_b32_e32 v5, 48, v0
	s_add_i32 s16, s25, 0x10000
	s_mov_b32 s17, m0
	s_mov_b32 m0, s16
	s_nop 0
	global_load_lds_dwordx4 v102, s[14:15]
	s_mov_b32 m0, s17
	v_lshl_or_b32 v98, v1, 6, v5
	s_waitcnt vmcnt(6) lgkmcnt(0)
	s_barrier
	v_lshl_or_b32 v103, v4, 6, v5
	ds_read_b128 v[28:31], v98
	ds_read_b128 v[24:27], v98 offset:1024
	ds_read_b128 v[16:19], v98 offset:2048
	ds_read_b128 v[0:3], v98 offset:3072
	ds_read_b128 v[20:23], v103 offset:16384
	ds_read_b128 v[12:15], v103 offset:17408
	ds_read_b128 v[8:11], v103 offset:18432
	ds_read_b128 v[4:7], v103 offset:19456
	s_add_u32 s14, s4, 0x180000
	v_mov_b32_e32 v84, 0
	s_movk_i32 s29, 0x6000
	v_or_b32_e32 v101, 0x4000, v103
	s_addc_u32 s15, s5, 0
	s_mul_hi_i32 s27, s12, 0xc0
	s_mul_i32 s28, s12, 0xc0
	s_lshl_b64 s[16:17], s[12:13], 7
	s_lshl_b64 s[18:19], s[12:13], 8
	s_mov_b32 s30, 0x12000
	s_mov_b32 s13, -2
	s_mov_b64 s[20:21], s[6:7]
	v_mov_b32_e32 v85, v84
	v_mov_b32_e32 v86, v84
	v_mov_b32_e32 v87, v84
	v_mov_b32_e32 v32, v84
	v_mov_b32_e32 v33, v84
	v_mov_b32_e32 v34, v84
	v_mov_b32_e32 v35, v84
	v_mov_b32_e32 v36, v84
	v_mov_b32_e32 v37, v84
	v_mov_b32_e32 v38, v84
	v_mov_b32_e32 v39, v84
	v_mov_b32_e32 v40, v84
	v_mov_b32_e32 v41, v84
	v_mov_b32_e32 v42, v84
	v_mov_b32_e32 v43, v84
	v_mov_b32_e32 v44, v84
	v_mov_b32_e32 v45, v84
	v_mov_b32_e32 v46, v84
	v_mov_b32_e32 v47, v84
	v_mov_b32_e32 v52, v84
	v_mov_b32_e32 v53, v84
	v_mov_b32_e32 v54, v84
	v_mov_b32_e32 v55, v84
	v_mov_b32_e32 v48, v84
	v_mov_b32_e32 v49, v84
	v_mov_b32_e32 v50, v84
	v_mov_b32_e32 v51, v84
	v_mov_b32_e32 v56, v84
	v_mov_b32_e32 v57, v84
	v_mov_b32_e32 v58, v84
	v_mov_b32_e32 v59, v84
	v_mov_b32_e32 v60, v84
	v_mov_b32_e32 v61, v84
	v_mov_b32_e32 v62, v84
	v_mov_b32_e32 v63, v84
	v_mov_b32_e32 v64, v84
	v_mov_b32_e32 v65, v84
	v_mov_b32_e32 v66, v84
	v_mov_b32_e32 v67, v84
	v_mov_b32_e32 v68, v84
	v_mov_b32_e32 v69, v84
	v_mov_b32_e32 v70, v84
	v_mov_b32_e32 v71, v84
	v_mov_b32_e32 v72, v84
	v_mov_b32_e32 v73, v84
	v_mov_b32_e32 v74, v84
	v_mov_b32_e32 v75, v84
	v_mov_b32_e32 v76, v84
	v_mov_b32_e32 v77, v84
	v_mov_b32_e32 v78, v84
	v_mov_b32_e32 v79, v84
	v_mov_b32_e32 v80, v84
	v_mov_b32_e32 v81, v84
	v_mov_b32_e32 v82, v84
	v_mov_b32_e32 v83, v84
	v_mov_b32_e32 v88, v84
	v_mov_b32_e32 v89, v84
	v_mov_b32_e32 v90, v84
	v_mov_b32_e32 v91, v84
	v_mov_b32_e32 v92, v84
	v_mov_b32_e32 v93, v84
	v_mov_b32_e32 v94, v84
	v_mov_b32_e32 v95, v84
	s_add_i32 s40, s23, 0x0
	s_add_i32 s41, s23, 0x400
	s_add_i32 s48, s26, 0x0
	s_add_i32 s42, s23, 0x6000
	s_add_i32 s43, s23, 0x6400
	s_add_i32 s49, s26, 0x6000
	s_add_i32 s44, s23, 0xc000
	s_add_i32 s45, s23, 0xc400
	s_add_i32 s50, s26, 0xc000
	s_add_i32 s46, s23, 0x12000
	s_add_i32 s47, s23, 0x12400
	s_add_i32 s51, s26, 0x12000
	v_add_u32_e32 v164, 0xc000, v98
	v_add_u32_e32 v165, 0xc000, v103
.Lout_P:
	s_waitcnt vmcnt(3) lgkmcnt(0)
	s_barrier
	s_add_u32 s34, s20, s28
	s_addc_u32 s35, s21, s27
	s_waitcnt lgkmcnt(3)
	v_mfma_f32_16x16x32_f16 v[92:95], v[20:23], v[28:31], v[92:95]
	v_mfma_f32_16x16x32_f16 v[72:75], v[20:23], v[24:27], v[72:75]
	s_mov_b32 m0, s46
	s_nop 0
	global_load_lds_dwordx4 v100, s[14:15]
	v_mfma_f32_16x16x32_f16 v[56:59], v[20:23], v[16:19], v[56:59]
	v_mfma_f32_16x16x32_f16 v[20:23], v[20:23], v[0:3], v[40:43]
	s_mov_b32 m0, s47
	s_nop 0
	global_load_lds_dwordx4 v99, s[14:15]
	s_waitcnt lgkmcnt(2)
	v_mfma_f32_16x16x32_f16 v[88:91], v[12:15], v[28:31], v[88:91]
	s_mov_b32 m0, s51
	s_nop 0
	global_load_lds_dwordx4 v102, s[34:35]
	s_waitcnt lgkmcnt(1)
	v_mfma_f32_16x16x32_f16 v[80:83], v[8:11], v[28:31], v[80:83]
	s_waitcnt lgkmcnt(0)
	v_mfma_f32_16x16x32_f16 v[28:31], v[4:7], v[28:31], v[76:79]
	s_add_u32 s30, s14, 0x80000
	s_addc_u32 s31, s15, 0
	s_add_u32 s34, s20, s18
	v_mfma_f32_16x16x32_f16 v[68:71], v[12:15], v[24:27], v[68:71]
	s_addc_u32 s35, s21, s19
	v_mfma_f32_16x16x32_f16 v[64:67], v[8:11], v[24:27], v[64:67]
	v_mfma_f32_16x16x32_f16 v[24:27], v[4:7], v[24:27], v[60:63]
	v_mfma_f32_16x16x32_f16 v[48:51], v[12:15], v[16:19], v[48:51]
	v_mfma_f32_16x16x32_f16 v[52:55], v[8:11], v[16:19], v[52:55]
	v_mfma_f32_16x16x32_f16 v[16:19], v[4:7], v[16:19], v[44:47]
	v_mfma_f32_16x16x32_f16 v[36:39], v[12:15], v[0:3], v[36:39]
	v_mfma_f32_16x16x32_f16 v[32:35], v[8:11], v[0:3], v[32:35]
	v_mfma_f32_16x16x32_f16 v[84:87], v[4:7], v[0:3], v[84:87]
	ds_read_b128 v[0:3], v103 offset:40960
	ds_read_b128 v[4:7], v103 offset:41984
	ds_read_b128 v[8:11], v98 offset:24576
	ds_read_b128 v[12:15], v98 offset:25600
	ds_read_b128 v[104:107], v103 offset:43008
	ds_read_b128 v[108:111], v103 offset:44032
	s_waitcnt lgkmcnt(3)
	v_mfma_f32_16x16x32_f16 v[92:95], v[0:3], v[8:11], v[92:95]
	v_mfma_f32_16x16x32_f16 v[88:91], v[4:7], v[8:11], v[88:91]
	s_waitcnt lgkmcnt(1)
	v_mfma_f32_16x16x32_f16 v[80:83], v[104:107], v[8:11], v[80:83]
	s_waitcnt lgkmcnt(0)
	v_mfma_f32_16x16x32_f16 v[76:79], v[108:111], v[8:11], v[28:31]
	ds_read_b128 v[8:11], v98 offset:26624
	ds_read_b128 v[112:115], v98 offset:27648
	s_waitcnt vmcnt(3) lgkmcnt(0)
	s_barrier
	v_mfma_f32_16x16x32_f16 v[72:75], v[0:3], v[12:15], v[72:75]
	v_mfma_f32_16x16x32_f16 v[68:71], v[4:7], v[12:15], v[68:71]
	s_mov_b32 m0, s40
	s_nop 0
	global_load_lds_dwordx4 v100, s[30:31]
	v_mfma_f32_16x16x32_f16 v[64:67], v[104:107], v[12:15], v[64:67]
	v_mfma_f32_16x16x32_f16 v[60:63], v[108:111], v[12:15], v[24:27]
	s_mov_b32 m0, s41
	s_nop 0
	global_load_lds_dwordx4 v99, s[30:31]
	s_add_i32 s13, s13, 2
	s_add_u32 s14, s14, 0x100000
	s_addc_u32 s15, s15, 0
	s_add_u32 s20, s20, s16
	s_addc_u32 s21, s21, s17
	s_waitcnt lgkmcnt(1)
	v_mfma_f32_16x16x32_f16 v[56:59], v[0:3], v[8:11], v[56:59]
	v_mfma_f32_16x16x32_f16 v[44:47], v[108:111], v[8:11], v[16:19]
	s_mov_b32 m0, s48
	s_nop 0
	global_load_lds_dwordx4 v102, s[34:35]
	s_cmp_gt_u32 s13, 25
	ds_read_b128 v[28:31], v164
	ds_read_b128 v[24:27], v164 offset:1024
	s_nop 0
	ds_read_b128 v[16:19], v164 offset:2048
	s_waitcnt lgkmcnt(3)
	v_mfma_f32_16x16x32_f16 v[40:43], v[0:3], v[112:115], v[20:23]
	ds_read_b128 v[0:3], v164 offset:3072
	s_nop 1
	ds_read_b128 v[20:23], v165 offset:16384
	ds_read_b128 v[12:15], v165 offset:17408
	v_mfma_f32_16x16x32_f16 v[48:51], v[4:7], v[8:11], v[48:51]
	v_mfma_f32_16x16x32_f16 v[52:55], v[104:107], v[8:11], v[52:55]
	v_mfma_f32_16x16x32_f16 v[36:39], v[4:7], v[112:115], v[36:39]
	ds_read_b128 v[8:11], v165 offset:18432
	ds_read_b128 v[4:7], v165 offset:19456
	v_mfma_f32_16x16x32_f16 v[32:35], v[104:107], v[112:115], v[32:35]
	v_mfma_f32_16x16x32_f16 v[84:87], v[108:111], v[112:115], v[84:87]
	s_cbranch_scc1 .Lout_exit
	s_waitcnt vmcnt(3) lgkmcnt(0)
	s_barrier
	s_add_u32 s34, s20, s28
	s_addc_u32 s35, s21, s27
	s_waitcnt lgkmcnt(3)
	v_mfma_f32_16x16x32_f16 v[92:95], v[20:23], v[28:31], v[92:95]
	v_mfma_f32_16x16x32_f16 v[72:75], v[20:23], v[24:27], v[72:75]
	s_mov_b32 m0, s42
	s_nop 0
	global_load_lds_dwordx4 v100, s[14:15]
	v_mfma_f32_16x16x32_f16 v[56:59], v[20:23], v[16:19], v[56:59]
	v_mfma_f32_16x16x32_f16 v[20:23], v[20:23], v[0:3], v[40:43]
	s_mov_b32 m0, s43
	s_nop 0
	global_load_lds_dwordx4 v99, s[14:15]
	s_waitcnt lgkmcnt(2)
	v_mfma_f32_16x16x32_f16 v[88:91], v[12:15], v[28:31], v[88:91]
	s_mov_b32 m0, s49
	s_nop 0
	global_load_lds_dwordx4 v102, s[34:35]
	s_waitcnt lgkmcnt(1)
	v_mfma_f32_16x16x32_f16 v[80:83], v[8:11], v[28:31], v[80:83]
	s_waitcnt lgkmcnt(0)
	v_mfma_f32_16x16x32_f16 v[28:31], v[4:7], v[28:31], v[76:79]
	s_add_u32 s30, s14, 0x80000
	s_addc_u32 s31, s15, 0
	s_add_u32 s34, s20, s18
	v_mfma_f32_16x16x32_f16 v[68:71], v[12:15], v[24:27], v[68:71]
	s_addc_u32 s35, s21, s19
	v_mfma_f32_16x16x32_f16 v[64:67], v[8:11], v[24:27], v[64:67]
	v_mfma_f32_16x16x32_f16 v[24:27], v[4:7], v[24:27], v[60:63]
	v_mfma_f32_16x16x32_f16 v[48:51], v[12:15], v[16:19], v[48:51]
	v_mfma_f32_16x16x32_f16 v[52:55], v[8:11], v[16:19], v[52:55]
	v_mfma_f32_16x16x32_f16 v[16:19], v[4:7], v[16:19], v[44:47]
	v_mfma_f32_16x16x32_f16 v[36:39], v[12:15], v[0:3], v[36:39]
	v_mfma_f32_16x16x32_f16 v[32:35], v[8:11], v[0:3], v[32:35]
	v_mfma_f32_16x16x32_f16 v[84:87], v[4:7], v[0:3], v[84:87]
	ds_read_b128 v[0:3], v165 offset:40960
	ds_read_b128 v[4:7], v165 offset:41984
	ds_read_b128 v[8:11], v164 offset:24576
	ds_read_b128 v[12:15], v164 offset:25600
	ds_read_b128 v[104:107], v165 offset:43008
	ds_read_b128 v[108:111], v165 offset:44032
	s_waitcnt lgkmcnt(3)
	v_mfma_f32_16x16x32_f16 v[92:95], v[0:3], v[8:11], v[92:95]
	v_mfma_f32_16x16x32_f16 v[88:91], v[4:7], v[8:11], v[88:91]
	s_waitcnt lgkmcnt(1)
	v_mfma_f32_16x16x32_f16 v[80:83], v[104:107], v[8:11], v[80:83]
	s_waitcnt lgkmcnt(0)
	v_mfma_f32_16x16x32_f16 v[76:79], v[108:111], v[8:11], v[28:31]
	ds_read_b128 v[8:11], v164 offset:26624
	ds_read_b128 v[112:115], v164 offset:27648
	s_waitcnt vmcnt(3) lgkmcnt(0)
	s_barrier
	v_mfma_f32_16x16x32_f16 v[72:75], v[0:3], v[12:15], v[72:75]
	v_mfma_f32_16x16x32_f16 v[68:71], v[4:7], v[12:15], v[68:71]
	s_mov_b32 m0, s44
	s_nop 0
	global_load_lds_dwordx4 v100, s[30:31]
	v_mfma_f32_16x16x32_f16 v[64:67], v[104:107], v[12:15], v[64:67]
	v_mfma_f32_16x16x32_f16 v[60:63], v[108:111], v[12:15], v[24:27]
	s_mov_b32 m0, s45
	s_nop 0
	global_load_lds_dwordx4 v99, s[30:31]
	s_add_i32 s13, s13, 2
	s_add_u32 s14, s14, 0x100000
	s_addc_u32 s15, s15, 0
	s_add_u32 s20, s20, s16
	s_addc_u32 s21, s21, s17
	s_waitcnt lgkmcnt(1)
	v_mfma_f32_16x16x32_f16 v[56:59], v[0:3], v[8:11], v[56:59]
	v_mfma_f32_16x16x32_f16 v[44:47], v[108:111], v[8:11], v[16:19]
	s_mov_b32 m0, s50
	s_nop 0
	global_load_lds_dwordx4 v102, s[34:35]
	s_cmp_gt_u32 s13, 25
	ds_read_b128 v[28:31], v98
	ds_read_b128 v[24:27], v98 offset:1024
	s_nop 0
	ds_read_b128 v[16:19], v98 offset:2048
	s_waitcnt lgkmcnt(3)
	v_mfma_f32_16x16x32_f16 v[40:43], v[0:3], v[112:115], v[20:23]
	ds_read_b128 v[0:3], v98 offset:3072
	s_nop 1
	ds_read_b128 v[20:23], v103 offset:16384
	ds_read_b128 v[12:15], v103 offset:17408
	v_mfma_f32_16x16x32_f16 v[48:51], v[4:7], v[8:11], v[48:51]
	v_mfma_f32_16x16x32_f16 v[52:55], v[104:107], v[8:11], v[52:55]
	v_mfma_f32_16x16x32_f16 v[36:39], v[4:7], v[112:115], v[36:39]
	ds_read_b128 v[8:11], v103 offset:18432
	ds_read_b128 v[4:7], v103 offset:19456
	v_mfma_f32_16x16x32_f16 v[32:35], v[104:107], v[112:115], v[32:35]
	v_mfma_f32_16x16x32_f16 v[84:87], v[108:111], v[112:115], v[84:87]
	s_cbranch_scc0 .Lout_P
.Lout_exit:
	s_lshl_b32 s13, s24, 8
	s_add_u32 s4, s4, 0xf80000
	s_addc_u32 s5, s5, 0
	s_mul_i32 s15, s12, 0x7c0
	s_waitcnt vmcnt(3) lgkmcnt(0)
	s_barrier
	s_mul_hi_i32 s14, s12, 0x7c0
	s_add_u32 s6, s6, s15
	s_addc_u32 s7, s7, s14
	s_add_i32 s14, s23, 0x12000
	s_mov_b32 s15, m0
	s_mov_b32 m0, s14
	s_nop 0
	global_load_lds_dwordx4 v100, s[4:5]
	s_mov_b32 m0, s15
	s_add_i32 s23, s23, 0x12400
	s_mov_b32 s14, m0
	s_mov_b32 m0, s23
	s_nop 0
	global_load_lds_dwordx4 v99, s[4:5]
	s_mov_b32 m0, s14
	s_add_i32 s25, s25, 0x16000
	s_mov_b32 s4, m0
	s_mov_b32 m0, s25
	s_nop 0
	global_load_lds_dwordx4 v102, s[6:7]
	s_mov_b32 m0, s4
	s_waitcnt lgkmcnt(3)
	v_mfma_f32_16x16x32_f16 v[92:95], v[20:23], v[28:31], v[92:95]
	v_lshlrev_b32_e32 v97, 3, v97
	v_and_or_b32 v97, v97, 24, s22
	v_or_b32_e32 v126, s2, v97
	s_waitcnt lgkmcnt(2)
	v_mfma_f32_16x16x32_f16 v[88:91], v[12:15], v[28:31], v[88:91]
	v_ashrrev_i32_e32 v127, 31, v126
	v_add_u32_e32 v99, 0x12400, v101
	v_add_u32_e32 v122, 0x12c00, v101
	s_waitcnt lgkmcnt(1)
	v_mfma_f32_16x16x32_f16 v[80:83], v[8:11], v[28:31], v[80:83]
	v_lshlrev_b64 v[138:139], 2, v[126:127]
	v_lshl_add_u64 v[134:135], s[10:11], 0, v[138:139]
	s_load_dword s0, s[0:1], 0x2c
	s_waitcnt lgkmcnt(0)
	v_mfma_f32_16x16x32_f16 v[28:31], v[4:7], v[28:31], v[76:79]
	s_add_i32 s3, s3, s13
	v_or_b32_e32 v140, s3, v96
	v_mad_i64_i32 v[96:97], s[2:3], v140, s12, 0
	v_mfma_f32_16x16x32_f16 v[72:75], v[20:23], v[24:27], v[72:75]
	v_lshl_add_u64 v[96:97], v[96:97], 2, s[8:9]
	v_lshl_add_u64 v[96:97], v[96:97], 0, v[138:139]
	v_mfma_f32_16x16x32_f16 v[68:71], v[12:15], v[24:27], v[68:71]
	v_mfma_f32_16x16x32_f16 v[64:67], v[8:11], v[24:27], v[64:67]
	v_mfma_f32_16x16x32_f16 v[24:27], v[4:7], v[24:27], v[60:63]
	v_mfma_f32_16x16x32_f16 v[56:59], v[20:23], v[16:19], v[56:59]
	v_mfma_f32_16x16x32_f16 v[48:51], v[12:15], v[16:19], v[48:51]
	v_mfma_f32_16x16x32_f16 v[52:55], v[8:11], v[16:19], v[52:55]
	v_mfma_f32_16x16x32_f16 v[16:19], v[4:7], v[16:19], v[44:47]
	v_mfma_f32_16x16x32_f16 v[20:23], v[20:23], v[0:3], v[40:43]
	v_mfma_f32_16x16x32_f16 v[12:15], v[12:15], v[0:3], v[36:39]
	v_mfma_f32_16x16x32_f16 v[8:11], v[8:11], v[0:3], v[32:35]
	s_nop 2
	ds_read_b128 v[32:35], v103 offset:40960
	ds_read_b128 v[36:39], v103 offset:41984
	v_mfma_f32_16x16x32_f16 v[0:3], v[4:7], v[0:3], v[84:87]
	ds_read_b128 v[4:7], v98 offset:24576
	ds_read_b128 v[40:43], v98 offset:25600
	ds_read_b128 v[60:63], v103 offset:43008
	ds_read_b128 v[84:87], v103 offset:44032
	s_waitcnt lgkmcnt(3)
	v_mfma_f32_16x16x32_f16 v[44:47], v[32:35], v[4:7], v[92:95]
	v_mfma_f32_16x16x32_f16 v[76:79], v[36:39], v[4:7], v[88:91]
	s_waitcnt lgkmcnt(1)
	v_mfma_f32_16x16x32_f16 v[80:83], v[60:63], v[4:7], v[80:83]
	s_waitcnt lgkmcnt(0)
	v_mfma_f32_16x16x32_f16 v[28:31], v[84:87], v[4:7], v[28:31]
	v_mfma_f32_16x16x32_f16 v[72:75], v[32:35], v[40:43], v[72:75]
	v_mfma_f32_16x16x32_f16 v[68:71], v[36:39], v[40:43], v[68:71]
	v_mfma_f32_16x16x32_f16 v[64:67], v[60:63], v[40:43], v[64:67]
	v_mfma_f32_16x16x32_f16 v[24:27], v[84:87], v[40:43], v[24:27]
	ds_read_b128 v[4:7], v98 offset:26624
	ds_read_b128 v[40:43], v98 offset:27648
	s_waitcnt vmcnt(3) lgkmcnt(0)
	s_barrier
	s_waitcnt lgkmcnt(1)
	v_mfma_f32_16x16x32_f16 v[56:59], v[32:35], v[4:7], v[56:59]
	s_waitcnt lgkmcnt(0)
	v_mfma_f32_16x16x32_f16 v[20:23], v[32:35], v[40:43], v[20:23]
	ds_read_b128 v[32:35], v101 offset:49152
	v_mfma_f32_16x16x32_f16 v[48:51], v[36:39], v[4:7], v[48:51]
	v_mfma_f32_16x16x32_f16 v[52:55], v[60:63], v[4:7], v[52:55]
	v_mfma_f32_16x16x32_f16 v[16:19], v[84:87], v[4:7], v[16:19]
	v_mfma_f32_16x16x32_f16 v[12:15], v[36:39], v[40:43], v[12:15]
	v_mfma_f32_16x16x32_f16 v[36:39], v[60:63], v[40:43], v[8:11]
	ds_read_b128 v[60:63], v98 offset:49152
	ds_read_b128 v[88:91], v98 offset:50176
	ds_read_b128 v[92:95], v101 offset:50176
	v_mfma_f32_16x16x32_f16 v[4:7], v[84:87], v[40:43], v[0:3]
	ds_read_b128 v[40:43], v98 offset:51200
	ds_read_b128 v[8:11], v98 offset:52224
	ds_read_b128 v[84:87], v101 offset:51200
	ds_read_b128 v[102:105], v101 offset:52224
	s_waitcnt vmcnt(0) lgkmcnt(0)
	s_barrier
	v_add_u32_e32 v0, 0x12000, v98
	v_add_u32_e32 v1, 0x12400, v98
	ds_read_b128 v[106:109], v0
	ds_read_b128 v[110:113], v1
	v_add_u32_e32 v0, 0x12800, v98
	v_add_u32_e32 v1, 0x12c00, v98
	v_add_u32_e32 v98, 0x12000, v101
	s_waitcnt lgkmcnt(8)
	v_mfma_f32_16x16x32_f16 v[44:47], v[32:35], v[60:63], v[44:47]
	ds_read_b128 v[114:117], v0
	ds_read_b128 v[0:3], v1
	s_waitcnt lgkmcnt(8)
	v_mfma_f32_16x16x32_f16 v[76:79], v[92:95], v[60:63], v[76:79]
	s_waitcnt lgkmcnt(5)
	v_mfma_f32_16x16x32_f16 v[80:83], v[84:87], v[60:63], v[80:83]
	s_waitcnt lgkmcnt(4)
	v_mfma_f32_16x16x32_f16 v[28:31], v[102:105], v[60:63], v[28:31]
	ds_read_b128 v[60:63], v98
	ds_read_b128 v[118:121], v99
	v_add_u32_e32 v98, 0x12800, v101
	ds_read_b128 v[98:101], v98
	ds_read_b128 v[122:125], v122
	s_waitcnt vmcnt(0) lgkmcnt(0)
	s_barrier
	global_load_dwordx4 v[148:151], v[134:135], off
	global_load_dwordx4 v[152:155], v[134:135], off offset:16
	global_load_dwordx4 v[156:159], v[134:135], off offset:128
	global_load_dwordx4 v[160:163], v[134:135], off offset:144
	v_and_b32_e32 v141, 24, v126
	v_lshlrev_b32_e32 v141, 1, v141
	v_sub_u32_e32 v138, v138, v141
	v_mfma_f32_16x16x32_f16 v[72:75], v[32:35], v[88:91], v[72:75]
	v_mfma_f32_16x16x32_f16 v[68:71], v[92:95], v[88:91], v[68:71]
	v_mfma_f32_16x16x32_f16 v[64:67], v[84:87], v[88:91], v[64:67]
	v_mfma_f32_16x16x32_f16 v[24:27], v[102:105], v[88:91], v[24:27]
	v_mfma_f32_16x16x32_f16 v[56:59], v[32:35], v[40:43], v[56:59]
	v_mfma_f32_16x16x32_f16 v[48:51], v[92:95], v[40:43], v[48:51]
	v_mfma_f32_16x16x32_f16 v[52:55], v[84:87], v[40:43], v[52:55]
	v_mfma_f32_16x16x32_f16 v[16:19], v[102:105], v[40:43], v[16:19]
	v_mfma_f32_16x16x32_f16 v[20:23], v[32:35], v[8:11], v[20:23]
	v_mfma_f32_16x16x32_f16 v[12:15], v[92:95], v[8:11], v[12:15]
	v_mfma_f32_16x16x32_f16 v[36:39], v[84:87], v[8:11], v[36:39]
	v_mfma_f32_16x16x32_f16 v[4:7], v[102:105], v[8:11], v[4:7]
	v_mad_i64_i32 v[96:97], s[2:3], v140, s12, 0
	v_lshl_add_u64 v[96:97], v[96:97], 2, s[8:9]
	v_lshl_add_u64 v[96:97], v[96:97], 0, v[138:139]
	v_or_b32_e32 v141, 16, v140
	v_mad_i64_i32 v[142:143], s[2:3], v141, s12, 0
	v_lshl_add_u64 v[142:143], v[142:143], 2, s[8:9]
	v_lshl_add_u64 v[142:143], v[142:143], 0, v[138:139]
	v_or_b32_e32 v141, 32, v140
	v_mad_i64_i32 v[144:145], s[2:3], v141, s12, 0
	v_lshl_add_u64 v[144:145], v[144:145], 2, s[8:9]
	v_lshl_add_u64 v[144:145], v[144:145], 0, v[138:139]
	v_or_b32_e32 v141, 48, v140
	v_mad_i64_i32 v[146:147], s[2:3], v141, s12, 0
	v_lshl_add_u64 v[146:147], v[146:147], 2, s[8:9]
	v_lshl_add_u64 v[146:147], v[146:147], 0, v[138:139]
	v_mfma_f32_16x16x32_f16 v[44:47], v[60:63], v[106:109], v[44:47]
	v_mfma_f32_16x16x32_f16 v[76:79], v[118:121], v[106:109], v[76:79]
	v_mfma_f32_16x16x32_f16 v[80:83], v[98:101], v[106:109], v[80:83]
	v_mfma_f32_16x16x32_f16 v[28:31], v[122:125], v[106:109], v[28:31]
	v_mfma_f32_16x16x32_f16 v[72:75], v[60:63], v[110:113], v[72:75]
	v_mfma_f32_16x16x32_f16 v[68:71], v[118:121], v[110:113], v[68:71]
	v_mfma_f32_16x16x32_f16 v[64:67], v[98:101], v[110:113], v[64:67]
	v_mfma_f32_16x16x32_f16 v[24:27], v[122:125], v[110:113], v[24:27]
	v_mfma_f32_16x16x32_f16 v[56:59], v[60:63], v[114:117], v[56:59]
	v_mfma_f32_16x16x32_f16 v[48:51], v[118:121], v[114:117], v[48:51]
	v_mfma_f32_16x16x32_f16 v[52:55], v[98:101], v[114:117], v[52:55]
	v_mfma_f32_16x16x32_f16 v[16:19], v[122:125], v[114:117], v[16:19]
	v_mfma_f32_16x16x32_f16 v[20:23], v[60:63], v[0:3], v[20:23]
	v_mfma_f32_16x16x32_f16 v[12:15], v[118:121], v[0:3], v[12:15]
	v_mfma_f32_16x16x32_f16 v[36:39], v[98:101], v[0:3], v[36:39]
	v_mfma_f32_16x16x32_f16 v[4:7], v[122:125], v[0:3], v[4:7]
	s_waitcnt vmcnt(0)
	v_pk_fma_f32 v[44:45], s[0:1], v[44:45], v[148:149] op_sel_hi:[0,1,1]
	v_pk_fma_f32 v[46:47], s[0:1], v[46:47], v[150:151] op_sel_hi:[0,1,1]
	v_pk_fma_f32 v[76:77], s[0:1], v[76:77], v[152:153] op_sel_hi:[0,1,1]
	v_pk_fma_f32 v[78:79], s[0:1], v[78:79], v[154:155] op_sel_hi:[0,1,1]
	v_pk_fma_f32 v[80:81], s[0:1], v[80:81], v[156:157] op_sel_hi:[0,1,1]
	v_pk_fma_f32 v[82:83], s[0:1], v[82:83], v[158:159] op_sel_hi:[0,1,1]
	v_pk_fma_f32 v[28:29], s[0:1], v[28:29], v[160:161] op_sel_hi:[0,1,1]
	v_pk_fma_f32 v[30:31], s[0:1], v[30:31], v[162:163] op_sel_hi:[0,1,1]
	s_nop 1
	v_permlane16_swap_b32_e32 v44, v76
	v_permlane16_swap_b32_e32 v45, v77
	v_permlane16_swap_b32_e32 v46, v78
	v_permlane16_swap_b32_e32 v47, v79
	v_permlane16_swap_b32_e32 v80, v28
	v_permlane16_swap_b32_e32 v81, v29
	v_permlane16_swap_b32_e32 v82, v30
	v_permlane16_swap_b32_e32 v83, v31
	v_permlane32_swap_b32_e32 v44, v76
	v_permlane32_swap_b32_e32 v45, v77
	v_permlane32_swap_b32_e32 v46, v78
	v_permlane32_swap_b32_e32 v47, v79
	v_permlane32_swap_b32_e32 v80, v28
	v_permlane32_swap_b32_e32 v81, v29
	v_permlane32_swap_b32_e32 v82, v30
	v_permlane32_swap_b32_e32 v83, v31
	global_store_dwordx4 v[96:97], v[44:47], off sc1
	global_store_dwordx4 v[96:97], v[76:79], off offset:64 sc1
	global_store_dwordx4 v[96:97], v[80:83], off offset:128 sc1
	global_store_dwordx4 v[96:97], v[28:31], off offset:192 sc1
	v_pk_fma_f32 v[72:73], s[0:1], v[72:73], v[148:149] op_sel_hi:[0,1,1]
	v_pk_fma_f32 v[74:75], s[0:1], v[74:75], v[150:151] op_sel_hi:[0,1,1]
	v_pk_fma_f32 v[68:69], s[0:1], v[68:69], v[152:153] op_sel_hi:[0,1,1]
	v_pk_fma_f32 v[70:71], s[0:1], v[70:71], v[154:155] op_sel_hi:[0,1,1]
	v_pk_fma_f32 v[64:65], s[0:1], v[64:65], v[156:157] op_sel_hi:[0,1,1]
	v_pk_fma_f32 v[66:67], s[0:1], v[66:67], v[158:159] op_sel_hi:[0,1,1]
	v_pk_fma_f32 v[24:25], s[0:1], v[24:25], v[160:161] op_sel_hi:[0,1,1]
	v_pk_fma_f32 v[26:27], s[0:1], v[26:27], v[162:163] op_sel_hi:[0,1,1]
	s_nop 1
	v_permlane16_swap_b32_e32 v72, v68
	v_permlane16_swap_b32_e32 v73, v69
	v_permlane16_swap_b32_e32 v74, v70
	v_permlane16_swap_b32_e32 v75, v71
	v_permlane16_swap_b32_e32 v64, v24
	v_permlane16_swap_b32_e32 v65, v25
	v_permlane16_swap_b32_e32 v66, v26
	v_permlane16_swap_b32_e32 v67, v27
	v_permlane32_swap_b32_e32 v72, v68
	v_permlane32_swap_b32_e32 v73, v69
	v_permlane32_swap_b32_e32 v74, v70
	v_permlane32_swap_b32_e32 v75, v71
	v_permlane32_swap_b32_e32 v64, v24
	v_permlane32_swap_b32_e32 v65, v25
	v_permlane32_swap_b32_e32 v66, v26
	v_permlane32_swap_b32_e32 v67, v27
	global_store_dwordx4 v[142:143], v[72:75], off sc1
	global_store_dwordx4 v[142:143], v[68:71], off offset:64 sc1
	global_store_dwordx4 v[142:143], v[64:67], off offset:128 sc1
	global_store_dwordx4 v[142:143], v[24:27], off offset:192 sc1
	v_pk_fma_f32 v[56:57], s[0:1], v[56:57], v[148:149] op_sel_hi:[0,1,1]
	v_pk_fma_f32 v[58:59], s[0:1], v[58:59], v[150:151] op_sel_hi:[0,1,1]
	v_pk_fma_f32 v[48:49], s[0:1], v[48:49], v[152:153] op_sel_hi:[0,1,1]
	v_pk_fma_f32 v[50:51], s[0:1], v[50:51], v[154:155] op_sel_hi:[0,1,1]
	v_pk_fma_f32 v[52:53], s[0:1], v[52:53], v[156:157] op_sel_hi:[0,1,1]
	v_pk_fma_f32 v[54:55], s[0:1], v[54:55], v[158:159] op_sel_hi:[0,1,1]
	v_pk_fma_f32 v[16:17], s[0:1], v[16:17], v[160:161] op_sel_hi:[0,1,1]
	v_pk_fma_f32 v[18:19], s[0:1], v[18:19], v[162:163] op_sel_hi:[0,1,1]
	s_nop 1
	v_permlane16_swap_b32_e32 v56, v48
	v_permlane16_swap_b32_e32 v57, v49
	v_permlane16_swap_b32_e32 v58, v50
	v_permlane16_swap_b32_e32 v59, v51
	v_permlane16_swap_b32_e32 v52, v16
	v_permlane16_swap_b32_e32 v53, v17
	v_permlane16_swap_b32_e32 v54, v18
	v_permlane16_swap_b32_e32 v55, v19
	v_permlane32_swap_b32_e32 v56, v48
	v_permlane32_swap_b32_e32 v57, v49
	v_permlane32_swap_b32_e32 v58, v50
	v_permlane32_swap_b32_e32 v59, v51
	v_permlane32_swap_b32_e32 v52, v16
	v_permlane32_swap_b32_e32 v53, v17
	v_permlane32_swap_b32_e32 v54, v18
	v_permlane32_swap_b32_e32 v55, v19
	global_store_dwordx4 v[144:145], v[56:59], off sc1
	global_store_dwordx4 v[144:145], v[48:51], off offset:64 sc1
	global_store_dwordx4 v[144:145], v[52:55], off offset:128 sc1
	global_store_dwordx4 v[144:145], v[16:19], off offset:192 sc1
	v_pk_fma_f32 v[20:21], s[0:1], v[20:21], v[148:149] op_sel_hi:[0,1,1]
	v_pk_fma_f32 v[22:23], s[0:1], v[22:23], v[150:151] op_sel_hi:[0,1,1]
	v_pk_fma_f32 v[12:13], s[0:1], v[12:13], v[152:153] op_sel_hi:[0,1,1]
	v_pk_fma_f32 v[14:15], s[0:1], v[14:15], v[154:155] op_sel_hi:[0,1,1]
	v_pk_fma_f32 v[36:37], s[0:1], v[36:37], v[156:157] op_sel_hi:[0,1,1]
	v_pk_fma_f32 v[38:39], s[0:1], v[38:39], v[158:159] op_sel_hi:[0,1,1]
	v_pk_fma_f32 v[4:5], s[0:1], v[4:5], v[160:161] op_sel_hi:[0,1,1]
	v_pk_fma_f32 v[6:7], s[0:1], v[6:7], v[162:163] op_sel_hi:[0,1,1]
	s_nop 1
	v_permlane16_swap_b32_e32 v20, v12
	v_permlane16_swap_b32_e32 v21, v13
	v_permlane16_swap_b32_e32 v22, v14
	v_permlane16_swap_b32_e32 v23, v15
	v_permlane16_swap_b32_e32 v36, v4
	v_permlane16_swap_b32_e32 v37, v5
	v_permlane16_swap_b32_e32 v38, v6
	v_permlane16_swap_b32_e32 v39, v7
	v_permlane32_swap_b32_e32 v20, v12
	v_permlane32_swap_b32_e32 v21, v13
	v_permlane32_swap_b32_e32 v22, v14
	v_permlane32_swap_b32_e32 v23, v15
	v_permlane32_swap_b32_e32 v36, v4
	v_permlane32_swap_b32_e32 v37, v5
	v_permlane32_swap_b32_e32 v38, v6
	v_permlane32_swap_b32_e32 v39, v7
	global_store_dwordx4 v[146:147], v[20:23], off sc1
	global_store_dwordx4 v[146:147], v[12:15], off offset:64 sc1
	global_store_dwordx4 v[146:147], v[36:39], off offset:128 sc1
	global_store_dwordx4 v[146:147], v[4:7], off offset:192 sc1
	s_endpgm
